# agg side-role transpose: 16 row loads in flight instead of one round trip per row; dtype comment; otherwise as previous (3 hand-written B-stationary f16-MFMA GEMMs, fragment-major weights)
# speedup vs baseline: 1.0845x; 1.0089x over previous
.LBB1_32:
	s_lshr_b32 s0, s8, 6
	s_ff1_i32_b32 s1, s0
	s_and_b32 s2, s2, 0xff
	s_lshr_b32 s9, s2, s1
	v_lshrrev_b32_e32 v3, 6, v0
	v_and_b32_e32 v2, 63, v0
	s_add_i32 s0, s0, -1
	v_lshl_or_b32 v0, s9, 6, v3
	s_and_b32 s10, s2, s0
	v_mul_u32_u24_e32 v0, s8, v0
	s_lshl_b32 s0, s10, 8
	s_mov_b32 s1, 0
	v_lshlrev_b32_e32 v6, 2, v0
	v_mov_b32_e32 v7, 0
	v_lshl_add_u64 v[0:1], s[0:1], 0, v[6:7]
	v_lshlrev_b32_e32 v6, 2, v2
	v_lshl_add_u64 v[0:1], v[0:1], 0, v[6:7]
	s_movk_i32 s2, 0x104
	v_or_b32_e32 v4, -4, v3
	s_waitcnt lgkmcnt(0)
	v_lshl_add_u64 v[0:1], s[6:7], 0, v[0:1]
	s_lshl_b32 s0, s8, 4
	v_mad_u32_u24 v5, v3, s2, v6
	s_mov_b64 s[2:3], 0
	global_load_dword v6, v[0:1], off nt
	v_lshl_add_u64 v[0:1], v[0:1], 0, s[0:1]
	global_load_dword v7, v[0:1], off nt
	v_lshl_add_u64 v[0:1], v[0:1], 0, s[0:1]
	global_load_dword v8, v[0:1], off nt
	v_lshl_add_u64 v[0:1], v[0:1], 0, s[0:1]
	global_load_dword v9, v[0:1], off nt
	v_lshl_add_u64 v[0:1], v[0:1], 0, s[0:1]
	global_load_dword v10, v[0:1], off nt
	v_lshl_add_u64 v[0:1], v[0:1], 0, s[0:1]
	global_load_dword v11, v[0:1], off nt
	v_lshl_add_u64 v[0:1], v[0:1], 0, s[0:1]
	global_load_dword v12, v[0:1], off nt
	v_lshl_add_u64 v[0:1], v[0:1], 0, s[0:1]
	global_load_dword v13, v[0:1], off nt
	v_lshl_add_u64 v[0:1], v[0:1], 0, s[0:1]
	global_load_dword v14, v[0:1], off nt
	v_lshl_add_u64 v[0:1], v[0:1], 0, s[0:1]
	global_load_dword v15, v[0:1], off nt
	v_lshl_add_u64 v[0:1], v[0:1], 0, s[0:1]
	global_load_dword v16, v[0:1], off nt
	v_lshl_add_u64 v[0:1], v[0:1], 0, s[0:1]
	global_load_dword v17, v[0:1], off nt
	v_lshl_add_u64 v[0:1], v[0:1], 0, s[0:1]
	global_load_dword v18, v[0:1], off nt
	v_lshl_add_u64 v[0:1], v[0:1], 0, s[0:1]
	global_load_dword v19, v[0:1], off nt
	v_lshl_add_u64 v[0:1], v[0:1], 0, s[0:1]
	global_load_dword v20, v[0:1], off nt
	v_lshl_add_u64 v[0:1], v[0:1], 0, s[0:1]
	global_load_dword v21, v[0:1], off nt
	s_waitcnt vmcnt(0)
	ds_write_b32 v5, v6
	ds_write_b32 v5, v7 offset:1040
	ds_write_b32 v5, v8 offset:2080
	ds_write_b32 v5, v9 offset:3120
	ds_write_b32 v5, v10 offset:4160
	ds_write_b32 v5, v11 offset:5200
	ds_write_b32 v5, v12 offset:6240
	ds_write_b32 v5, v13 offset:7280
	ds_write_b32 v5, v14 offset:8320
	ds_write_b32 v5, v15 offset:9360
	ds_write_b32 v5, v16 offset:10400
	ds_write_b32 v5, v17 offset:11440
	ds_write_b32 v5, v18 offset:12480
	ds_write_b32 v5, v19 offset:13520
	ds_write_b32 v5, v20 offset:14560
	ds_write_b32 v5, v21 offset:15600
	v_lshlrev_b32_e32 v0, 8, v2
	v_lshl_or_b32 v0, v2, 2, v0
	v_lshl_add_u32 v4, v3, 2, v0
	s_waitcnt lgkmcnt(0)
	s_barrier
	ds_read2_b32 v[6:7], v4 offset1:4
	ds_read2_b32 v[8:9], v4 offset0:8 offset1:12
	ds_read2_b32 v[10:11], v4 offset0:16 offset1:20
	ds_read2_b32 v[12:13], v4 offset0:24 offset1:28
	ds_read2_b32 v[14:15], v4 offset0:32 offset1:36
	ds_read2_b32 v[16:17], v4 offset0:40 offset1:44
	ds_read2_b32 v[18:19], v4 offset0:48 offset1:52
	ds_read2_b32 v[20:21], v4 offset0:56 offset1:60
	v_bfe_u32 v0, v2, 3, 2
	v_lshlrev_b32_e32 v0, 8, v0
	v_and_b32_e32 v1, 7, v2
	v_lshl_or_b32 v0, v1, 1, v0
	v_lshl_or_b32 v0, v3, 4, v0
	v_lshrrev_b32_e32 v1, 5, v2
	s_waitcnt lgkmcnt(0)
	v_cvt_f16_f32_e32 v6, v6
	v_cvt_f16_f32_e32 v7, v7
	v_cvt_f16_f32_e32 v8, v8
	v_cvt_f16_f32_e32 v9, v9
	v_cvt_f16_f32_e32 v10, v10
	v_cvt_f16_f32_e32 v11, v11
	v_cvt_f16_f32_e32 v12, v12
	v_cvt_f16_f32_e32 v13, v13
	v_cvt_f16_f32_e32 v14, v14
	v_cvt_f16_f32_e32 v15, v15
	v_cvt_f16_f32_e32 v16, v16
	v_cvt_f16_f32_e32 v17, v17
	v_cvt_f16_f32_e32 v18, v18
	v_cvt_f16_f32_e32 v19, v19
	v_cvt_f16_f32_e32 v20, v20
	v_cvt_f16_f32_e32 v21, v21
	s_cmpk_eq_u32 s8, 0x200
	s_cbranch_scc1 .Lagg_w2t
	v_lshl_or_b32 v0, v1, 12, v0
	s_lshl_b32 s0, s10, 16
	s_lshl_b32 s1, s9, 13
	s_add_i32 s0, s0, s1
	s_add_u32 s4, s4, s0
	s_addc_u32 s5, s5, 0
	global_store_short v0, v6, s[4:5]
	global_store_short v0, v7, s[4:5] offset:1024
	global_store_short v0, v8, s[4:5] offset:2048
	global_store_short v0, v9, s[4:5] offset:3072
	global_store_short v0, v10, s[4:5] offset:64
	global_store_short v0, v11, s[4:5] offset:1088
	global_store_short v0, v12, s[4:5] offset:2112
	global_store_short v0, v13, s[4:5] offset:3136
	global_store_short v0, v14, s[4:5] offset:128
	global_store_short v0, v15, s[4:5] offset:1152
	global_store_short v0, v16, s[4:5] offset:2176
	global_store_short v0, v17, s[4:5] offset:3200
	global_store_short v0, v18, s[4:5] offset:192
	global_store_short v0, v19, s[4:5] offset:1216
	global_store_short v0, v20, s[4:5] offset:2240
	global_store_short v0, v21, s[4:5] offset:3264
	s_endpgm
